# P4 (out GEMM): first half K-iteration peeled with C=0 MFMAs, no accumulator zeroing movs; on top of sgu load masking + K swizzle
# baseline (speedup 1.0000x reference)
; #define PG8_STAGE(bufoff, gbase, voff) do { _Pragma("unroll") for (int _i = 0; _i < 2; ++_i) \
;         __builtin_amdgcn_global_load_lds((const unsigned*)((const char*)(gbase) + (voff)[_i]), (PG8_LAS unsigned*)(lds + (bufoff) + ldsw + _i * 8192), 16, 0, 0); } while (0)
; #define PG8_LDA(dst, b, h) do { _Pragma("unroll") for (int m = 0; m < 4; ++m) _Pragma("unroll") for (int k = 0; k < 2; ++k) dst[m][k] = *(const PG8_LAS bf16x8*)(lds + PG8_SA(b, h) + aoff + m * 2048 + k * 1024); } while (0)
; #define PG8_LDB(dst, b, h) do { _Pragma("unroll") for (int n = 0; n < 2; ++n) _Pragma("unroll") for (int k = 0; k < 2; ++k) dst[n][k] = *(const PG8_LAS bf16x8*)(lds + PG8_SB(b, h) + boff + n * 2048 + k * 1024); } while (0)
; #define PG8_MMA(ai, bj, At, Bt) do { __builtin_amdgcn_s_setprio(1); _Pragma("unroll") for (int m = 0; m < 4; ++m) _Pragma("unroll") for (int n = 0; n < 2; ++n) _Pragma("unroll") for (int k = 0; k < 2; ++k) \
;         acc[ai][bj][m][n] = __builtin_amdgcn_mfma_f32_16x16x32_bf16(Bt[n][k], At[m][k], acc[ai][bj][m][n], 0, 0, 0); __builtin_amdgcn_s_setprio(0); } while (0)
; #define PG8_WAIT_V(n) asm volatile("s_waitcnt vmcnt(" #n ")" ::: "memory")
; #define PG8_WAIT_L(n) asm volatile("s_waitcnt lgkmcnt(" #n ")" ::: "memory")
; template <class Epi, class Sched, bool ALIGN_EPI = false, bool SP2 = false>
; __device__ __forceinline__ void gemm_phase(PG8_LAS unsigned char* lds, const Gemm g, const Sched& S, const Epi& E) {
;     ...
;             const char* a2 = last ? nA : cA + (size_t)(t + 2) * kstep; const char* b2 = last ? nB : cB + (size_t)(t + 2) * kstep;
;             const char* a3 = a2 + kstep; const char* b3 = b2 + kstep;
;             if (last && has_next) S.a_ready(nxt);
;             if constexpr (Epi::HAS_MID) { if (t != 0 && (t & (Epi::MID_EVERY - 1)) == 0) E.mid(acc, cur, t / Epi::MID_EVERY, wr, wc, fr, fq); }
;             if constexpr (SP2) {
;             PG8_LDB(B0, 0, 0); PG8_LDB(B1, 0, 1); PG8_SCHED; PG8_LDA(At, 0, 0); PG8_STAGE(PG8_SA(1, 1), a1 + hstep, voffA);
;             PG8_WAIT_V(8); PG8_WAIT_L(0); PG8_BAR; PG8_MMA(0, 0, At, B0); PG8_MMA(0, 1, At, B1); PG8_BAR; PG8_SCHED;
;             PG8_LDA(At, 0, 1); PG8_STAGE(PG8_SB(0, 0), b2, voffB); PG8_STAGE(PG8_SB(0, 1), b2 + hstep, voffB); PG8_STAGE(PG8_SA(0, 0), a2, voffA);
;             PG8_WAIT_V(8); PG8_WAIT_L(0); PG8_BAR; PG8_MMA(1, 0, At, B0); PG8_MMA(1, 1, At, B1); PG8_BAR; PG8_SCHED;
.LBB0_1679:
	s_ashr_i32 s17, s16, 31
	s_lshl_b64 s[18:19], s[16:17], 21
	s_add_u32 s18, s2, s18
	s_addc_u32 s19, s26, s19
	s_and_b64 s[20:21], s[4:5], exec
	s_cselect_b32 s17, s19, s13
	s_cselect_b32 s41, s18, s12
	s_ashr_i32 s15, s14, 31
	s_lshl_b64 s[20:21], s[14:15], 21
	s_add_u32 s20, s27, s20
	s_addc_u32 s21, s28, s21
	s_and_b64 s[24:25], s[4:5], exec
	s_cselect_b32 s15, s21, s23
	s_cselect_b32 s42, s20, s22
	s_add_u32 s12, s12, 0x100080
	s_addc_u32 s13, s13, 0
	s_add_u32 s43, s22, 0x100
	s_addc_u32 s44, s23, 0
	s_mov_b32 s45, -2
	s_add_u32 s22, s12, 0xfff00080
	s_addc_u32 s23, s13, -1
	s_add_i32 s46, 0, 0x10000
	s_cmp_eq_u32 s45, 60
	s_cselect_b32 s25, s17, s23
	s_cselect_b32 s24, s41, s22
	s_cselect_b32 s23, s15, s44
	s_cselect_b32 s22, s42, s43
	s_add_i32 s48, 0, 0x14000
	v_add_u32_e32 v152, s46, v176
	v_add_u32_e32 v168, s48, v176
	ds_read_b128 v[140:143], v152
	ds_read_b128 v[144:147], v152 offset:1024
	ds_read_b128 v[148:151], v152 offset:256
	ds_read_b128 v[152:155], v152 offset:1280
	ds_read_b128 v[156:159], v168
	ds_read_b128 v[160:163], v168 offset:1024
	ds_read_b128 v[164:167], v168 offset:256
	ds_read_b128 v[168:171], v168 offset:1280
	v_lshl_add_u64 v[210:211], s[12:13], 0, v[136:137]
	s_add_i32 m0, s30, 0xc000
	ds_read_b128 v[172:175], v180
	ds_read_b128 v[182:185], v180 offset:1024
	ds_read_b128 v[186:189], v180 offset:2048
	ds_read_b128 v[190:193], v180 offset:3072
	ds_read_b128 v[194:197], v180 offset:4096
	ds_read_b128 v[198:201], v180 offset:5120
	ds_read_b128 v[202:205], v180 offset:6144
	ds_read_b128 v[206:209], v180 offset:7168
	global_load_lds_dwordx4 v[210:211], off
	v_lshl_add_u64 v[210:211], s[12:13], 0, v[138:139]
	s_add_i32 m0, s30, 0xe000
	s_nop 0
	global_load_lds_dwordx4 v[210:211], off
	s_waitcnt vmcnt(8)
	s_waitcnt lgkmcnt(0)
	s_barrier
	s_setprio 1
	s_waitcnt lgkmcnt(0)
	v_mfma_f32_16x16x32_bf16 v[128:131], v[140:143], v[172:175], 0
	v_mfma_f32_16x16x32_bf16 v[124:127], v[148:151], v[172:175], 0
	v_mfma_f32_16x16x32_bf16 v[112:115], v[140:143], v[186:189], 0
	v_mfma_f32_16x16x32_bf16 v[108:111], v[148:151], v[186:189], 0
	v_mfma_f32_16x16x32_bf16 v[96:99], v[140:143], v[194:197], 0
	v_mfma_f32_16x16x32_bf16 v[92:95], v[148:151], v[194:197], 0
	v_mfma_f32_16x16x32_bf16 v[80:83], v[140:143], v[202:205], 0
	v_mfma_f32_16x16x32_bf16 v[76:79], v[148:151], v[202:205], 0
	v_mfma_f32_16x16x32_bf16 v[128:131], v[144:147], v[182:185], v[128:131]
	v_mfma_f32_16x16x32_bf16 v[124:127], v[152:155], v[182:185], v[124:127]
	v_mfma_f32_16x16x32_bf16 v[112:115], v[144:147], v[190:193], v[112:115]
	v_mfma_f32_16x16x32_bf16 v[108:111], v[152:155], v[190:193], v[108:111]
	v_mfma_f32_16x16x32_bf16 v[96:99], v[144:147], v[198:201], v[96:99]
	v_mfma_f32_16x16x32_bf16 v[92:95], v[152:155], v[198:201], v[92:95]
	v_mfma_f32_16x16x32_bf16 v[80:83], v[144:147], v[206:209], v[80:83]
	v_mfma_f32_16x16x32_bf16 v[76:79], v[152:155], v[206:209], v[76:79]
	s_setprio 0
	s_setprio 1
	v_mfma_f32_16x16x32_bf16 v[120:123], v[156:159], v[172:175], 0
	v_mfma_f32_16x16x32_bf16 v[116:119], v[164:167], v[172:175], 0
	v_mfma_f32_16x16x32_bf16 v[104:107], v[156:159], v[186:189], 0
	v_mfma_f32_16x16x32_bf16 v[100:103], v[164:167], v[186:189], 0
	v_mfma_f32_16x16x32_bf16 v[88:91], v[156:159], v[194:197], 0
	v_mfma_f32_16x16x32_bf16 v[84:87], v[164:167], v[194:197], 0
	v_mfma_f32_16x16x32_bf16 v[72:75], v[156:159], v[202:205], 0
	v_mfma_f32_16x16x32_bf16 v[68:71], v[164:167], v[202:205], 0
	v_mfma_f32_16x16x32_bf16 v[120:123], v[160:163], v[182:185], v[120:123]
	v_mfma_f32_16x16x32_bf16 v[116:119], v[168:171], v[182:185], v[116:119]
	v_mfma_f32_16x16x32_bf16 v[104:107], v[160:163], v[190:193], v[104:107]
	v_mfma_f32_16x16x32_bf16 v[100:103], v[168:171], v[190:193], v[100:103]
	v_mfma_f32_16x16x32_bf16 v[88:91], v[160:163], v[198:201], v[88:91]
	v_mfma_f32_16x16x32_bf16 v[84:87], v[168:171], v[198:201], v[84:87]
	v_mfma_f32_16x16x32_bf16 v[72:75], v[160:163], v[206:209], v[72:75]
	v_mfma_f32_16x16x32_bf16 v[68:71], v[168:171], v[206:209], v[68:71]
	s_setprio 0
	s_barrier
; #define PG8_STAGE(bufoff, gbase, voff) do { _Pragma("unroll") for (int _i = 0; _i < 2; ++_i) \
;         __builtin_amdgcn_global_load_lds((const unsigned*)((const char*)(gbase) + (voff)[_i]), (PG8_LAS unsigned*)(lds + (bufoff) + ldsw + _i * 8192), 16, 0, 0); } while (0)
; #define PG8_LDA(dst, b, h) do { _Pragma("unroll") for (int m = 0; m < 4; ++m) _Pragma("unroll") for (int k = 0; k < 2; ++k) dst[m][k] = *(const PG8_LAS bf16x8*)(lds + PG8_SA(b, h) + aoff + m * 2048 + k * 1024); } while (0)
; #define PG8_MMA(ai, bj, At, Bt) do { __builtin_amdgcn_s_setprio(1); _Pragma("unroll") for (int m = 0; m < 4; ++m) _Pragma("unroll") for (int n = 0; n < 2; ++n) _Pragma("unroll") for (int k = 0; k < 2; ++k) \
;         acc[ai][bj][m][n] = __builtin_amdgcn_mfma_f32_16x16x32_bf16(Bt[n][k], At[m][k], acc[ai][bj][m][n], 0, 0, 0); __builtin_amdgcn_s_setprio(0); } while (0)
; #define PG8_WAIT_V(n) asm volatile("s_waitcnt vmcnt(" #n ")" ::: "memory")
; #define PG8_WAIT_L(n) asm volatile("s_waitcnt lgkmcnt(" #n ")" ::: "memory")
; #define PG8_BAR __builtin_amdgcn_s_barrier()
; #define PG8_SCHED __builtin_amdgcn_sched_barrier(0)
; template <class Epi, class Sched, bool ALIGN_EPI = false, bool SP2 = false>
; __device__ __forceinline__ void gemm_phase(PG8_LAS unsigned char* lds, const Gemm g, const Sched& S, const Epi& E) {
;     ...
;             PG8_LDA(At, 0, 1); PG8_STAGE(PG8_SB(0, 0), b2, voffB); PG8_STAGE(PG8_SB(0, 1), b2 + hstep, voffB); PG8_STAGE(PG8_SA(0, 0), a2, voffA);
;             PG8_WAIT_V(8); PG8_WAIT_L(0); PG8_BAR; PG8_MMA(1, 0, At, B0); PG8_MMA(1, 1, At, B1); PG8_BAR; PG8_SCHED;
	s_add_i32 s46, s46, s29
	v_lshl_add_u64 v[210:211], s[22:23], 0, v[2:3]
	s_mov_b32 m0, s46
	ds_read_b128 v[172:175], v180 offset:16384
	ds_read_b128 v[182:185], v180 offset:17408
	ds_read_b128 v[186:189], v180 offset:18432
	ds_read_b128 v[190:193], v180 offset:19456
	ds_read_b128 v[194:197], v180 offset:20480
	ds_read_b128 v[198:201], v180 offset:21504
	ds_read_b128 v[202:205], v180 offset:22528
	ds_read_b128 v[206:209], v180 offset:23552
	global_load_lds_dwordx4 v[210:211], off
	s_add_i32 m0, s46, 0x2000
	s_add_u32 s46, s22, 0x100000
	v_lshl_add_u64 v[212:213], s[22:23], 0, v[132:133]
	s_addc_u32 s47, s23, 0
	s_add_i32 s48, s48, s29
	global_load_lds_dwordx4 v[212:213], off
	v_lshl_add_u64 v[214:215], s[46:47], 0, v[2:3]
	s_mov_b32 m0, s48
	v_lshl_add_u64 v[216:217], s[24:25], 0, v[132:133]
	global_load_lds_dwordx4 v[214:215], off
	v_lshl_add_u64 v[214:215], s[46:47], 0, v[132:133]
	s_add_i32 m0, s48, 0x2000
	s_nop 0
	global_load_lds_dwordx4 v[214:215], off
	v_lshl_add_u64 v[214:215], s[24:25], 0, v[2:3]
	s_mov_b32 m0, s30
	s_nop 0
	global_load_lds_dwordx4 v[214:215], off
	s_mov_b32 m0, s31
	s_nop 0
	global_load_lds_dwordx4 v[216:217], off
	s_waitcnt vmcnt(8)
	s_waitcnt lgkmcnt(0)
	s_barrier
	s_setprio 1
	s_waitcnt lgkmcnt(0)
	v_mfma_f32_16x16x32_bf16 v[64:67], v[140:143], v[172:175], 0
	v_mfma_f32_16x16x32_bf16 v[60:63], v[148:151], v[172:175], 0
	v_mfma_f32_16x16x32_bf16 v[48:51], v[140:143], v[186:189], 0
	v_mfma_f32_16x16x32_bf16 v[44:47], v[148:151], v[186:189], 0
	v_mfma_f32_16x16x32_bf16 v[32:35], v[140:143], v[194:197], 0
	v_mfma_f32_16x16x32_bf16 v[28:31], v[148:151], v[194:197], 0
	v_mfma_f32_16x16x32_bf16 v[16:19], v[140:143], v[202:205], 0
	v_mfma_f32_16x16x32_bf16 v[12:15], v[148:151], v[202:205], 0
	v_mfma_f32_16x16x32_bf16 v[64:67], v[144:147], v[182:185], v[64:67]
	v_mfma_f32_16x16x32_bf16 v[60:63], v[152:155], v[182:185], v[60:63]
	v_mfma_f32_16x16x32_bf16 v[48:51], v[144:147], v[190:193], v[48:51]
	v_mfma_f32_16x16x32_bf16 v[44:47], v[152:155], v[190:193], v[44:47]
	v_mfma_f32_16x16x32_bf16 v[32:35], v[144:147], v[198:201], v[32:35]
	v_mfma_f32_16x16x32_bf16 v[28:31], v[152:155], v[198:201], v[28:31]
	v_mfma_f32_16x16x32_bf16 v[16:19], v[144:147], v[206:209], v[16:19]
	v_mfma_f32_16x16x32_bf16 v[12:15], v[152:155], v[206:209], v[12:15]
	s_setprio 0
	s_setprio 1
	v_mfma_f32_16x16x32_bf16 v[56:59], v[156:159], v[172:175], 0
	v_mfma_f32_16x16x32_bf16 v[52:55], v[164:167], v[172:175], 0
	v_mfma_f32_16x16x32_bf16 v[40:43], v[156:159], v[186:189], 0
	v_mfma_f32_16x16x32_bf16 v[36:39], v[164:167], v[186:189], 0
	v_mfma_f32_16x16x32_bf16 v[24:27], v[156:159], v[194:197], 0
	v_mfma_f32_16x16x32_bf16 v[20:23], v[164:167], v[194:197], 0
	v_mfma_f32_16x16x32_bf16 v[8:11], v[156:159], v[202:205], 0
	v_mfma_f32_16x16x32_bf16 v[4:7], v[164:167], v[202:205], 0
	v_mfma_f32_16x16x32_bf16 v[56:59], v[160:163], v[182:185], v[56:59]
	v_mfma_f32_16x16x32_bf16 v[52:55], v[168:171], v[182:185], v[52:55]
	v_mfma_f32_16x16x32_bf16 v[40:43], v[160:163], v[190:193], v[40:43]
	v_mfma_f32_16x16x32_bf16 v[36:39], v[168:171], v[190:193], v[36:39]
	v_mfma_f32_16x16x32_bf16 v[24:27], v[160:163], v[198:201], v[24:27]
	v_mfma_f32_16x16x32_bf16 v[20:23], v[168:171], v[198:201], v[20:23]
	v_mfma_f32_16x16x32_bf16 v[8:11], v[160:163], v[206:209], v[8:11]
	v_mfma_f32_16x16x32_bf16 v[4:7], v[168:171], v[206:209], v[4:7]
	s_setprio 0
	s_barrier
	s_branch .Lp4_kloop_mid

; #define PG8_STAGE(bufoff, gbase, voff) do { _Pragma("unroll") for (int _i = 0; _i < 2; ++_i) \
;         __builtin_amdgcn_global_load_lds((const unsigned*)((const char*)(gbase) + (voff)[_i]), (PG8_LAS unsigned*)(lds + (bufoff) + ldsw + _i * 8192), 16, 0, 0); } while (0)
; #define PG8_LDA(dst, b, h) do { _Pragma("unroll") for (int m = 0; m < 4; ++m) _Pragma("unroll") for (int k = 0; k < 2; ++k) dst[m][k] = *(const PG8_LAS bf16x8*)(lds + PG8_SA(b, h) + aoff + m * 2048 + k * 1024); } while (0)
; #define PG8_LDB(dst, b, h) do { _Pragma("unroll") for (int n = 0; n < 2; ++n) _Pragma("unroll") for (int k = 0; k < 2; ++k) dst[n][k] = *(const PG8_LAS bf16x8*)(lds + PG8_SB(b, h) + boff + n * 2048 + k * 1024); } while (0)
; #define PG8_MMA(ai, bj, At, Bt) do { __builtin_amdgcn_s_setprio(1); _Pragma("unroll") for (int m = 0; m < 4; ++m) _Pragma("unroll") for (int n = 0; n < 2; ++n) _Pragma("unroll") for (int k = 0; k < 2; ++k) \
;         acc[ai][bj][m][n] = __builtin_amdgcn_mfma_f32_16x16x32_bf16(Bt[n][k], At[m][k], acc[ai][bj][m][n], 0, 0, 0); __builtin_amdgcn_s_setprio(0); } while (0)
; #define PG8_WAIT_V(n) asm volatile("s_waitcnt vmcnt(" #n ")" ::: "memory")
; #define PG8_WAIT_L(n) asm volatile("s_waitcnt lgkmcnt(" #n ")" ::: "memory")
; #define PG8_BAR __builtin_amdgcn_s_barrier()
; #define PG8_SCHED __builtin_amdgcn_sched_barrier(0)
; template <class Epi, class Sched, bool ALIGN_EPI = false, bool SP2 = false>
; __device__ __forceinline__ void gemm_phase(PG8_LAS unsigned char* lds, const Gemm g, const Sched& S, const Epi& E) {
;     ...
;             PG8_LDB(B0, 1, 0); PG8_LDB(B1, 1, 1); PG8_SCHED; PG8_LDA(At, 1, 0); PG8_STAGE(PG8_SA(0, 1), a2 + hstep, voffA);
;             PG8_WAIT_V(8); PG8_WAIT_L(0); PG8_BAR; PG8_MMA(0, 0, At, B0); PG8_MMA(0, 1, At, B1); PG8_BAR; PG8_SCHED;
.Lp4_kloop_mid:
	s_add_i32 s46, 0, 0x18000
	s_add_i32 s47, 0, 0x1c000
	v_add_u32_e32 v152, s46, v176
	v_add_u32_e32 v168, s47, v176
	ds_read_b128 v[140:143], v152
	ds_read_b128 v[144:147], v152 offset:1024
	ds_read_b128 v[148:151], v152 offset:256
	ds_read_b128 v[152:155], v152 offset:1280
	ds_read_b128 v[156:159], v168
	ds_read_b128 v[160:163], v168 offset:1024
	ds_read_b128 v[164:167], v168 offset:256
	ds_read_b128 v[168:171], v168 offset:1280
	s_add_u32 s24, s24, 0x100000
	s_addc_u32 s25, s25, 0
	s_mov_b32 m0, s34
	v_lshl_add_u64 v[222:223], s[24:25], 0, v[2:3]
	ds_read_b128 v[172:175], v180 offset:32768
	ds_read_b128 v[182:185], v180 offset:33792
	ds_read_b128 v[186:189], v180 offset:34816
	ds_read_b128 v[190:193], v180 offset:35840
	ds_read_b128 v[194:197], v180 offset:36864
	ds_read_b128 v[198:201], v180 offset:37888
	ds_read_b128 v[202:205], v180 offset:38912
	ds_read_b128 v[206:209], v180 offset:39936
	global_load_lds_dwordx4 v[222:223], off
	v_lshl_add_u64 v[222:223], s[24:25], 0, v[132:133]
	s_mov_b32 m0, s35
	s_nop 0
	global_load_lds_dwordx4 v[222:223], off
	s_waitcnt vmcnt(8)
	s_waitcnt lgkmcnt(0)
	s_barrier
	s_setprio 1
	s_waitcnt lgkmcnt(0)
	v_mfma_f32_16x16x32_bf16 v[128:131], v[140:143], v[172:175], v[128:131]
	v_mfma_f32_16x16x32_bf16 v[124:127], v[148:151], v[172:175], v[124:127]
	v_mfma_f32_16x16x32_bf16 v[112:115], v[140:143], v[186:189], v[112:115]
	v_mfma_f32_16x16x32_bf16 v[108:111], v[148:151], v[186:189], v[108:111]
	v_mfma_f32_16x16x32_bf16 v[96:99], v[140:143], v[194:197], v[96:99]
	v_mfma_f32_16x16x32_bf16 v[92:95], v[148:151], v[194:197], v[92:95]
	v_mfma_f32_16x16x32_bf16 v[80:83], v[140:143], v[202:205], v[80:83]
	v_mfma_f32_16x16x32_bf16 v[76:79], v[148:151], v[202:205], v[76:79]
	v_mfma_f32_16x16x32_bf16 v[128:131], v[144:147], v[182:185], v[128:131]
	v_mfma_f32_16x16x32_bf16 v[124:127], v[152:155], v[182:185], v[124:127]
	v_mfma_f32_16x16x32_bf16 v[112:115], v[144:147], v[190:193], v[112:115]
	v_mfma_f32_16x16x32_bf16 v[108:111], v[152:155], v[190:193], v[108:111]
	v_mfma_f32_16x16x32_bf16 v[96:99], v[144:147], v[198:201], v[96:99]
	v_mfma_f32_16x16x32_bf16 v[92:95], v[152:155], v[198:201], v[92:95]
	v_mfma_f32_16x16x32_bf16 v[80:83], v[144:147], v[206:209], v[80:83]
	v_mfma_f32_16x16x32_bf16 v[76:79], v[152:155], v[206:209], v[76:79]
	s_setprio 0
	s_setprio 1
	v_mfma_f32_16x16x32_bf16 v[120:123], v[156:159], v[172:175], v[120:123]
	v_mfma_f32_16x16x32_bf16 v[116:119], v[164:167], v[172:175], v[116:119]
	v_mfma_f32_16x16x32_bf16 v[104:107], v[156:159], v[186:189], v[104:107]
	v_mfma_f32_16x16x32_bf16 v[100:103], v[164:167], v[186:189], v[100:103]
	v_mfma_f32_16x16x32_bf16 v[88:91], v[156:159], v[194:197], v[88:91]
	v_mfma_f32_16x16x32_bf16 v[84:87], v[164:167], v[194:197], v[84:87]
	v_mfma_f32_16x16x32_bf16 v[72:75], v[156:159], v[202:205], v[72:75]
	v_mfma_f32_16x16x32_bf16 v[68:71], v[164:167], v[202:205], v[68:71]
	v_mfma_f32_16x16x32_bf16 v[120:123], v[160:163], v[182:185], v[120:123]
	v_mfma_f32_16x16x32_bf16 v[116:119], v[168:171], v[182:185], v[116:119]
	v_mfma_f32_16x16x32_bf16 v[104:107], v[160:163], v[190:193], v[104:107]
	v_mfma_f32_16x16x32_bf16 v[100:103], v[168:171], v[190:193], v[100:103]
	v_mfma_f32_16x16x32_bf16 v[88:91], v[160:163], v[198:201], v[88:91]
	v_mfma_f32_16x16x32_bf16 v[84:87], v[168:171], v[198:201], v[84:87]
	v_mfma_f32_16x16x32_bf16 v[72:75], v[160:163], v[206:209], v[72:75]
	v_mfma_f32_16x16x32_bf16 v[68:71], v[168:171], v[206:209], v[68:71]
	s_setprio 0
	s_barrier
; #define PG8_STAGE(bufoff, gbase, voff) do { _Pragma("unroll") for (int _i = 0; _i < 2; ++_i) \
;         __builtin_amdgcn_global_load_lds((const unsigned*)((const char*)(gbase) + (voff)[_i]), (PG8_LAS unsigned*)(lds + (bufoff) + ldsw + _i * 8192), 16, 0, 0); } while (0)
; #define PG8_LDA(dst, b, h) do { _Pragma("unroll") for (int m = 0; m < 4; ++m) _Pragma("unroll") for (int k = 0; k < 2; ++k) dst[m][k] = *(const PG8_LAS bf16x8*)(lds + PG8_SA(b, h) + aoff + m * 2048 + k * 1024); } while (0)
; #define PG8_WAIT_V(n) asm volatile("s_waitcnt vmcnt(" #n ")" ::: "memory")
; template <class Epi, class Sched, bool ALIGN_EPI = false, bool SP2 = false>
; __device__ __forceinline__ void gemm_phase(PG8_LAS unsigned char* lds, const Gemm g, const Sched& S, const Epi& E) {
;     ...
;         for (int t = 0; t < nt; t += 2) {
;             const bool last = (t == nt - 2);
;             const char* a1 = cA + (size_t)(t + 1) * kstep;
;             const char* a2 = last ? nA : cA + (size_t)(t + 2) * kstep; const char* b2 = last ? nB : cB + (size_t)(t + 2) * kstep;
;             const char* a3 = a2 + kstep; const char* b3 = b2 + kstep;
;             if (last && has_next) S.a_ready(nxt);
;             if constexpr (Epi::HAS_MID) { if (t != 0 && (t & (Epi::MID_EVERY - 1)) == 0) E.mid(acc, cur, t / Epi::MID_EVERY, wr, wc, fr, fq); }
;             if constexpr (SP2) {
;             PG8_LDB(B0, 0, 0); PG8_LDB(B1, 0, 1); PG8_SCHED; PG8_LDA(At, 0, 0); PG8_STAGE(PG8_SA(1, 1), a1 + hstep, voffA);
;             PG8_WAIT_V(8); PG8_WAIT_L(0); PG8_BAR; PG8_MMA(0, 0, At, B0); PG8_MMA(0, 1, At, B1); PG8_BAR; PG8_SCHED;
;             PG8_LDA(At, 0, 1); PG8_STAGE(PG8_SB(0, 0), b2, voffB); PG8_STAGE(PG8_SB(0, 1), b2 + hstep, voffB); PG8_STAGE(PG8_SA(0, 0), a2, voffA);
;             PG8_WAIT_V(8); PG8_WAIT_L(0); PG8_BAR; PG8_MMA(1, 0, At, B0); PG8_MMA(1, 1, At, B1); PG8_BAR; PG8_SCHED;
;             PG8_LDB(B0, 1, 0); PG8_LDB(B1, 1, 1); PG8_SCHED; PG8_LDA(At, 1, 0); PG8_STAGE(PG8_SA(0, 1), a2 + hstep, voffA);
;             PG8_WAIT_V(8); PG8_WAIT_L(0); PG8_BAR; PG8_MMA(0, 0, At, B0); PG8_MMA(0, 1, At, B1); PG8_BAR; PG8_SCHED;
;             PG8_LDA(At, 1, 1); PG8_STAGE(PG8_SB(1, 0), b3, voffB); PG8_STAGE(PG8_SB(1, 1), b3 + hstep, voffB); PG8_STAGE(PG8_SA(1, 0), a3, voffA);
;             PG8_WAIT_V(8); PG8_WAIT_L(0); PG8_BAR; PG8_MMA(1, 0, At, B0); PG8_MMA(1, 1, At, B1); PG8_BAR; PG8_SCHED;
	s_add_i32 s24, s46, s29
	v_lshl_add_u64 v[210:211], v[210:211], 0, s[78:79]
	s_mov_b32 m0, s24
	ds_read_b128 v[172:175], v180 offset:49152
	ds_read_b128 v[182:185], v180 offset:50176
	ds_read_b128 v[186:189], v180 offset:51200
	ds_read_b128 v[190:193], v180 offset:52224
	ds_read_b128 v[194:197], v180 offset:53248
	ds_read_b128 v[198:201], v180 offset:54272
	ds_read_b128 v[202:205], v180 offset:55296
	ds_read_b128 v[206:209], v180 offset:56320
	global_load_lds_dwordx4 v[210:211], off
	s_add_i32 m0, s24, 0x2000
	s_add_u32 s22, s22, 0x100080
	v_lshl_add_u64 v[210:211], v[212:213], 0, s[78:79]
	s_addc_u32 s23, s23, 0
	s_add_i32 s24, s47, s29
	global_load_lds_dwordx4 v[210:211], off
	v_lshl_add_u64 v[210:211], s[22:23], 0, v[2:3]
	s_mov_b32 m0, s24
	s_nop 0
	global_load_lds_dwordx4 v[210:211], off
	v_lshl_add_u64 v[210:211], s[22:23], 0, v[132:133]
	s_add_i32 m0, s24, 0x2000
	s_nop 0
	global_load_lds_dwordx4 v[210:211], off
	v_lshl_add_u64 v[210:211], v[214:215], 0, s[78:79]
	s_mov_b32 m0, s37
	s_nop 0
	global_load_lds_dwordx4 v[210:211], off
	v_lshl_add_u64 v[210:211], v[216:217], 0, s[78:79]
	s_mov_b32 m0, s38
	s_nop 0
	global_load_lds_dwordx4 v[210:211], off
	s_waitcnt vmcnt(8)
	s_waitcnt lgkmcnt(0)
	s_barrier
	s_setprio 1
	s_waitcnt lgkmcnt(0)
	v_mfma_f32_16x16x32_bf16 v[64:67], v[140:143], v[172:175], v[64:67]
	v_mfma_f32_16x16x32_bf16 v[60:63], v[148:151], v[172:175], v[60:63]
	v_mfma_f32_16x16x32_bf16 v[48:51], v[140:143], v[186:189], v[48:51]
	v_mfma_f32_16x16x32_bf16 v[44:47], v[148:151], v[186:189], v[44:47]
	v_mfma_f32_16x16x32_bf16 v[32:35], v[140:143], v[194:197], v[32:35]
	v_mfma_f32_16x16x32_bf16 v[28:31], v[148:151], v[194:197], v[28:31]
	v_mfma_f32_16x16x32_bf16 v[16:19], v[140:143], v[202:205], v[16:19]
	v_mfma_f32_16x16x32_bf16 v[12:15], v[148:151], v[202:205], v[12:15]
	v_mfma_f32_16x16x32_bf16 v[64:67], v[144:147], v[182:185], v[64:67]
	v_mfma_f32_16x16x32_bf16 v[60:63], v[152:155], v[182:185], v[60:63]
	v_mfma_f32_16x16x32_bf16 v[48:51], v[144:147], v[190:193], v[48:51]
	v_mfma_f32_16x16x32_bf16 v[44:47], v[152:155], v[190:193], v[44:47]
	v_mfma_f32_16x16x32_bf16 v[32:35], v[144:147], v[198:201], v[32:35]
	v_mfma_f32_16x16x32_bf16 v[28:31], v[152:155], v[198:201], v[28:31]
	v_mfma_f32_16x16x32_bf16 v[16:19], v[144:147], v[206:209], v[16:19]
	v_mfma_f32_16x16x32_bf16 v[12:15], v[152:155], v[206:209], v[12:15]
	s_setprio 0
	s_setprio 1
	v_mfma_f32_16x16x32_bf16 v[56:59], v[156:159], v[172:175], v[56:59]
	v_mfma_f32_16x16x32_bf16 v[52:55], v[164:167], v[172:175], v[52:55]
	v_mfma_f32_16x16x32_bf16 v[40:43], v[156:159], v[186:189], v[40:43]
	v_mfma_f32_16x16x32_bf16 v[36:39], v[164:167], v[186:189], v[36:39]
	v_mfma_f32_16x16x32_bf16 v[24:27], v[156:159], v[194:197], v[24:27]
	v_mfma_f32_16x16x32_bf16 v[20:23], v[164:167], v[194:197], v[20:23]
	v_mfma_f32_16x16x32_bf16 v[8:11], v[156:159], v[202:205], v[8:11]
	v_mfma_f32_16x16x32_bf16 v[4:7], v[164:167], v[202:205], v[4:7]
	v_mfma_f32_16x16x32_bf16 v[56:59], v[160:163], v[182:185], v[56:59]
	v_mfma_f32_16x16x32_bf16 v[52:55], v[168:171], v[182:185], v[52:55]
	v_mfma_f32_16x16x32_bf16 v[40:43], v[160:163], v[190:193], v[40:43]
	v_mfma_f32_16x16x32_bf16 v[36:39], v[168:171], v[190:193], v[36:39]
	v_mfma_f32_16x16x32_bf16 v[24:27], v[160:163], v[198:201], v[24:27]
	v_mfma_f32_16x16x32_bf16 v[20:23], v[168:171], v[198:201], v[20:23]
	v_mfma_f32_16x16x32_bf16 v[8:11], v[160:163], v[206:209], v[8:11]
	v_mfma_f32_16x16x32_bf16 v[4:7], v[168:171], v[206:209], v[4:7]
	s_setprio 0
	s_barrier
	s_add_i32 s45, s45, 2
	s_add_u32 s12, s12, 0x100
	s_addc_u32 s13, s13, 0
	s_add_u32 s43, s43, 0x100
	s_addc_u32 s44, s44, 0
	s_cmp_gt_u32 s45, 61
	s_cbranch_scc0 .LBB0_1680
	s_and_b64 vcc, exec, s[10:11]
	s_cbranch_vccz .LBB0_1683
	s_barrier
